# attention tile loops: waves 4-7 staggered behind waves 0-3 by s_sleep 3 (192 cycles) after each tile barrier so the two waves of a SIMD de-overlap their MFMA and VALU phases
# speedup vs baseline: 1.0095x; 1.0034x over previous
.LBB0_1652:
	s_or_b64 exec, exec, s[8:9]
	s_barrier
	v_readfirstlane_b32 s101, v0
	s_bitcmp1_b32 s101, 8
	s_cbranch_scc0 .Lmy_stg_ma
	s_sleep 3

.LBB0_1707:
	s_or_b64 exec, exec, s[34:35]
	s_barrier
	v_readfirstlane_b32 s101, v0
	s_bitcmp1_b32 s101, 8
	s_cbranch_scc0 .Lmy_stg_dl
	s_sleep 3
